# speedup vs baseline: 1.0051x; 1.0051x over previous
.Lmy_prio1:
.Lmy_attn_loop1:
	v_add_u32_e32 v252, s1, v158
	v_add_u32_e32 v253, 0x10800, v252
	s_waitcnt lgkmcnt(1)
	v_mfma_f32_32x32x16_bf16 v[80:95], v[196:199], v[112:115], 0
	ds_read_b128 v[128:131], v253 offset:0
	ds_read_b128 v[148:151], v253 offset:1024
	v_cvt_pk_bf16_f32 v186, v76, v77
	v_cvt_pk_bf16_f32 v187, v78, v79
	v_exp_f32_e32 v48, v48
	v_exp_f32_e32 v49, v49
	v_exp_f32_e32 v50, v50
	v_exp_f32_e32 v51, v51
	s_waitcnt lgkmcnt(2)
	v_mfma_f32_32x32x16_bf16 v[80:95], v[108:111], v[120:123], v[80:95]
	v_exp_f32_e32 v52, v52
	v_exp_f32_e32 v53, v53
	v_exp_f32_e32 v54, v54
	v_exp_f32_e32 v55, v55
	v_cvt_pk_bf16_f32 v172, v48, v49
	v_cvt_pk_bf16_f32 v173, v50, v51
	v_mfma_f32_16x16x32_bf16 v[140:143], v[96:99], v[180:183], v[140:143]
	v_mfma_f32_32x32x16_bf16 v[0:15], v[168:171], v[180:183], v[0:15]
	v_exp_f32_e32 v56, v56
	v_exp_f32_e32 v57, v57
	v_exp_f32_e32 v58, v58
	v_exp_f32_e32 v59, v59
	v_cvt_pk_bf16_f32 v174, v52, v53
	v_cvt_pk_bf16_f32 v175, v54, v55
	v_mfma_f32_32x32x16_bf16 v[0:15], v[248:251], v[184:187], v[0:15]
	v_exp_f32_e32 v60, v60
	v_exp_f32_e32 v61, v61
	v_exp_f32_e32 v62, v62
	v_exp_f32_e32 v63, v63
	v_cvt_pk_bf16_f32 v176, v56, v57
	v_cvt_pk_bf16_f32 v177, v58, v59
	v_mfma_f32_16x16x32_bf16 v[140:143], v[96:99], v[184:187], v[140:143]
	v_mfma_f32_32x32x16_bf16 v[64:79], v[196:199], v[116:119], 0
	ds_read_b128 v[188:191], v252 offset:4096
	ds_read_b128 v[192:195], v252 offset:5120
	v_cvt_pk_bf16_f32 v178, v60, v61
	v_cvt_pk_bf16_f32 v179, v62, v63
	v_exp_f32_e32 v32, v32
	v_exp_f32_e32 v33, v33
	v_exp_f32_e32 v34, v34
	v_exp_f32_e32 v35, v35
	v_mfma_f32_32x32x16_bf16 v[64:79], v[108:111], v[124:127], v[64:79]
	v_exp_f32_e32 v36, v36
	v_exp_f32_e32 v37, v37
	v_exp_f32_e32 v38, v38
	v_exp_f32_e32 v39, v39
	v_cvt_pk_bf16_f32 v180, v32, v33
	v_cvt_pk_bf16_f32 v181, v34, v35
	v_mfma_f32_16x16x32_bf16 v[144:147], v[96:99], v[172:175], v[144:147]
	s_waitcnt lgkmcnt(2)
	v_mfma_f32_32x32x16_bf16 v[16:31], v[128:131], v[172:175], v[16:31]
	v_exp_f32_e32 v40, v40
	v_exp_f32_e32 v41, v41
	v_exp_f32_e32 v42, v42
	v_exp_f32_e32 v43, v43
	v_cvt_pk_bf16_f32 v182, v36, v37
	v_cvt_pk_bf16_f32 v183, v38, v39
	v_mfma_f32_32x32x16_bf16 v[16:31], v[148:151], v[176:179], v[16:31]
	v_exp_f32_e32 v44, v44
	v_exp_f32_e32 v45, v45
	v_exp_f32_e32 v46, v46
	v_exp_f32_e32 v47, v47
	v_cvt_pk_bf16_f32 v184, v40, v41
	v_cvt_pk_bf16_f32 v185, v42, v43
	v_mfma_f32_16x16x32_bf16 v[144:147], v[96:99], v[176:179], v[144:147]
	s_waitcnt lgkmcnt(1)
	v_mfma_f32_32x32x16_bf16 v[48:63], v[188:191], v[112:115], 0
	ds_read_b128 v[168:171], v253 offset:2048
	ds_read_b128 v[248:251], v253 offset:3072
	v_cvt_pk_bf16_f32 v186, v44, v45
	v_cvt_pk_bf16_f32 v187, v46, v47
	v_exp_f32_e32 v80, v80
	v_exp_f32_e32 v81, v81
	v_exp_f32_e32 v82, v82
	v_exp_f32_e32 v83, v83
	s_waitcnt lgkmcnt(2)
	v_mfma_f32_32x32x16_bf16 v[48:63], v[192:195], v[120:123], v[48:63]
	v_exp_f32_e32 v84, v84
	v_exp_f32_e32 v85, v85
	v_exp_f32_e32 v86, v86
	v_exp_f32_e32 v87, v87
	v_cvt_pk_bf16_f32 v172, v80, v81
	v_cvt_pk_bf16_f32 v173, v82, v83
	v_mfma_f32_16x16x32_bf16 v[140:143], v[96:99], v[180:183], v[140:143]
	v_mfma_f32_32x32x16_bf16 v[0:15], v[128:131], v[180:183], v[0:15]
	v_exp_f32_e32 v88, v88
	v_exp_f32_e32 v89, v89
	v_exp_f32_e32 v90, v90
	v_exp_f32_e32 v91, v91
	v_cvt_pk_bf16_f32 v174, v84, v85
	v_cvt_pk_bf16_f32 v175, v86, v87
	v_mfma_f32_32x32x16_bf16 v[0:15], v[148:151], v[184:187], v[0:15]
	v_exp_f32_e32 v92, v92
	v_exp_f32_e32 v93, v93
	v_exp_f32_e32 v94, v94
	v_exp_f32_e32 v95, v95
	v_cvt_pk_bf16_f32 v176, v88, v89
	v_cvt_pk_bf16_f32 v177, v90, v91
	v_mfma_f32_16x16x32_bf16 v[140:143], v[96:99], v[184:187], v[140:143]
	v_mfma_f32_32x32x16_bf16 v[32:47], v[188:191], v[116:119], 0
	ds_read_b128 v[196:199], v252 offset:6144
	ds_read_b128 v[108:111], v252 offset:7168
	v_cvt_pk_bf16_f32 v178, v92, v93
	v_cvt_pk_bf16_f32 v179, v94, v95
	v_exp_f32_e32 v64, v64
	v_exp_f32_e32 v65, v65
	v_exp_f32_e32 v66, v66
	v_exp_f32_e32 v67, v67
	v_mfma_f32_32x32x16_bf16 v[32:47], v[192:195], v[124:127], v[32:47]
	v_exp_f32_e32 v68, v68
	v_exp_f32_e32 v69, v69
	v_exp_f32_e32 v70, v70
	v_exp_f32_e32 v71, v71
	v_cvt_pk_bf16_f32 v180, v64, v65
	v_cvt_pk_bf16_f32 v181, v66, v67
	v_mfma_f32_16x16x32_bf16 v[144:147], v[96:99], v[172:175], v[144:147]
	s_waitcnt lgkmcnt(2)
	v_mfma_f32_32x32x16_bf16 v[16:31], v[168:171], v[172:175], v[16:31]
	v_exp_f32_e32 v72, v72
	v_exp_f32_e32 v73, v73
	v_exp_f32_e32 v74, v74
	v_exp_f32_e32 v75, v75
	v_cvt_pk_bf16_f32 v182, v68, v69
	v_cvt_pk_bf16_f32 v183, v70, v71
	v_mfma_f32_32x32x16_bf16 v[16:31], v[248:251], v[176:179], v[16:31]
	v_exp_f32_e32 v76, v76
	v_exp_f32_e32 v77, v77
	v_exp_f32_e32 v78, v78
	v_exp_f32_e32 v79, v79
	v_cvt_pk_bf16_f32 v184, v72, v73
	v_cvt_pk_bf16_f32 v185, v74, v75
	v_mfma_f32_16x16x32_bf16 v[144:147], v[96:99], v[176:179], v[144:147]
	s_addk_i32 s1, 0x1000
	s_cmp_lg_u32 s1, 0x10000
	s_cbranch_scc1 .Lmy_attn_loop1
	v_cvt_pk_bf16_f32 v186, v76, v77
	v_cvt_pk_bf16_f32 v187, v78, v79
	v_mfma_f32_32x32x16_bf16 v[0:15], v[168:171], v[180:183], v[0:15]
	s_nop 0
	v_mfma_f32_16x16x32_bf16 v[140:143], v[96:99], v[180:183], v[140:143]
	v_mfma_f32_32x32x16_bf16 v[0:15], v[248:251], v[184:187], v[0:15]
	s_nop 0
	s_nop 1
	v_mfma_f32_16x16x32_bf16 v[140:143], v[96:99], v[184:187], v[140:143]
	v_lshrrev_b32_e32 v60, 2, v158
	v_and_b32_e32 v60, 60, v60
	v_and_b32_e32 v61, 0x100, v158
	v_lshrrev_b32_e32 v61, 1, v61
	v_or_b32_e32 v60, v60, v61
	s_nop 4
	ds_bpermute_b32 v61, v60, v140
	ds_bpermute_b32 v62, v60, v144
	s_waitcnt lgkmcnt(0)
	v_mul_f32_e32 v140, 0.5, v61
	v_mul_f32_e32 v144, 0.5, v62
	v_mov_b32_e32 v34, 0x3f80
	v_cmp_gt_u32_e64 s[0:1], 32, v154
	v_or_b32_e32 v36, 0x20c00, v158
	s_mov_b32 s2, 0x3f803f80
	v_cndmask_b32_e64 v96, 0, v34, s[0:1]
	v_or_b32_e32 v34, 0x20800, v158
	ds_read_b128 v[108:111], v34
	ds_read_b128 v[128:131], v36
	v_exp_f32_e32 v34, v48
	v_exp_f32_e32 v35, v49
	s_mov_b32 s3, s2
	v_mov_b64_e32 v[52:53], s[2:3]
	v_exp_f32_e32 v32, v32
	v_exp_f32_e32 v33, v33
	v_mov_b32_e32 v97, 0
	v_cndmask_b32_e64 v34, 0, v34, s[0:1]
	v_cndmask_b32_e64 v35, 0, v35, s[0:1]
	v_cvt_pk_bf16_f32 v34, v34, v35
	v_mov_b32_e32 v35, v97
	v_mov_b32_e32 v36, v97
	v_mov_b32_e32 v37, v97
	s_mov_b32 s8, 0
	v_cndmask_b32_e64 v32, 0, v32, s[0:1]
	v_cndmask_b32_e64 v33, 0, v33, s[0:1]
	s_waitcnt lgkmcnt(1)
	v_mfma_f32_32x32x16_bf16 v[16:31], v[108:111], v[34:37], v[16:31]
	s_mov_b32 s9, s8
	v_cvt_pk_bf16_f32 v46, v32, v33
	v_mov_b64_e32 v[50:51], s[8:9]
	v_mov_b32_e32 v32, v46
	v_mov_b32_e32 v33, v97
	v_mov_b32_e32 v47, v97
	v_mov_b32_e32 v48, v97
	v_mfma_f32_4x4x4_16b_bf16 v[34:37], v[52:53], v[34:35], v[144:147]
	v_mov_b32_e32 v49, v97
	s_mov_b32 s10, s8
	v_mfma_f32_4x4x4_16b_bf16 v[38:41], v[52:53], v[50:51], v[34:37]
	s_mov_b32 s11, s8
	v_mfma_f32_4x4x4_16b_bf16 v[32:35], v[52:53], v[32:33], v[140:143]
	v_mov_b64_e32 v[44:45], s[10:11]
	v_mfma_f32_32x32x16_bf16 v[0:15], v[108:111], v[46:49], v[0:15]
	v_mov_b64_e32 v[42:43], s[8:9]
	s_mov_b32 s7, 0x7149f2ca
	s_mov_b32 s4, 0xda24260
	v_mov_b32_e32 v98, v97
	v_mov_b32_e32 v99, v97
	v_mfma_f32_4x4x4_16b_bf16 v[32:35], v[52:53], v[50:51], v[32:35]
	s_waitcnt lgkmcnt(0)
	v_mfma_f32_32x32x16_bf16 v[16:31], v[128:131], v[42:45], v[16:31]
	s_nop 2
	v_mbcnt_lo_u32_b32 v33, -1, 0
	v_mbcnt_hi_u32_b32 v33, -1, v33
	v_and_b32_e32 v35, 64, v33
	v_xor_b32_e32 v34, 32, v33
	v_add_u32_e32 v35, 64, v35
	v_cmp_lt_i32_e32 vcc, v34, v35
	v_mfma_f32_32x32x16_bf16 v[0:15], v[128:131], v[42:45], v[0:15]
	s_nop 0
	v_cndmask_b32_e32 v33, v33, v34, vcc
	v_lshlrev_b32_e32 v165, 2, v33
	ds_bpermute_b32 v35, v165, v38
	ds_bpermute_b32 v34, v165, v32
	v_mov_b32_e32 v33, v38
	s_waitcnt lgkmcnt(0)
	v_pk_add_f32 v[34:35], v[32:33], v[34:35]
	s_nop 0
	v_cmp_ngt_f32_e32 vcc, s7, v35
	v_cmp_nlt_f32_e64 s[2:3], s4, v34
	v_cmp_nlt_f32_e64 s[4:5], s4, v35
	s_or_b64 s[4:5], s[4:5], vcc
	v_cmp_ngt_f32_e32 vcc, s7, v34
	s_or_b64 s[2:3], s[2:3], vcc
	s_or_b64 vcc, s[4:5], s[2:3]
	s_cbranch_vccnz .LBB6_40

.Lmy_prio2:
.Lmy_attn_loop2:
	v_add_u32_e32 v248, s27, v158
	v_add_u32_e32 v249, 0x10800, v248
	s_waitcnt lgkmcnt(1)
	v_mfma_f32_32x32x16_bf16 v[80:95], v[224:227], v[100:103], 0
	ds_read_b128 v[232:235], v249 offset:0
	ds_read_b128 v[236:239], v249 offset:1024
	v_cvt_pk_bf16_f32 v186, v76, v77
	v_cvt_pk_bf16_f32 v187, v78, v79
	v_exp_f32_e32 v48, v48
	v_exp_f32_e32 v49, v49
	v_exp_f32_e32 v50, v50
	v_exp_f32_e32 v51, v51
	s_waitcnt lgkmcnt(2)
	v_mfma_f32_32x32x16_bf16 v[80:95], v[228:231], v[108:111], v[80:95]
	v_exp_f32_e32 v52, v52
	v_exp_f32_e32 v53, v53
	v_exp_f32_e32 v54, v54
	v_exp_f32_e32 v55, v55
	v_cvt_pk_bf16_f32 v172, v48, v49
	v_cvt_pk_bf16_f32 v173, v50, v51
	v_mfma_f32_16x16x32_bf16 v[136:139], v[116:119], v[180:183], v[136:139]
	v_mfma_f32_32x32x16_bf16 v[0:15], v[240:243], v[180:183], v[0:15]
	v_exp_f32_e32 v56, v56
	v_exp_f32_e32 v57, v57
	v_exp_f32_e32 v58, v58
	v_exp_f32_e32 v59, v59
	v_cvt_pk_bf16_f32 v174, v52, v53
	v_cvt_pk_bf16_f32 v175, v54, v55
	v_mfma_f32_32x32x16_bf16 v[0:15], v[244:247], v[184:187], v[0:15]
	v_exp_f32_e32 v60, v60
	v_exp_f32_e32 v61, v61
	v_exp_f32_e32 v62, v62
	v_exp_f32_e32 v63, v63
	v_cvt_pk_bf16_f32 v176, v56, v57
	v_cvt_pk_bf16_f32 v177, v58, v59
	v_mfma_f32_16x16x32_bf16 v[136:139], v[116:119], v[184:187], v[136:139]
	v_mfma_f32_32x32x16_bf16 v[64:79], v[224:227], v[104:107], 0
	ds_read_b128 v[216:219], v248 offset:4096
	ds_read_b128 v[220:223], v248 offset:5120
	v_cvt_pk_bf16_f32 v178, v60, v61
	v_cvt_pk_bf16_f32 v179, v62, v63
	v_exp_f32_e32 v32, v32
	v_exp_f32_e32 v33, v33
	v_exp_f32_e32 v34, v34
	v_exp_f32_e32 v35, v35
	v_mfma_f32_32x32x16_bf16 v[64:79], v[228:231], v[112:115], v[64:79]
	v_exp_f32_e32 v36, v36
	v_exp_f32_e32 v37, v37
	v_exp_f32_e32 v38, v38
	v_exp_f32_e32 v39, v39
	v_cvt_pk_bf16_f32 v180, v32, v33
	v_cvt_pk_bf16_f32 v181, v34, v35
	v_mfma_f32_16x16x32_bf16 v[140:143], v[116:119], v[172:175], v[140:143]
	s_waitcnt lgkmcnt(2)
	v_mfma_f32_32x32x16_bf16 v[16:31], v[232:235], v[172:175], v[16:31]
	v_exp_f32_e32 v40, v40
	v_exp_f32_e32 v41, v41
	v_exp_f32_e32 v42, v42
	v_exp_f32_e32 v43, v43
	v_cvt_pk_bf16_f32 v182, v36, v37
	v_cvt_pk_bf16_f32 v183, v38, v39
	v_mfma_f32_32x32x16_bf16 v[16:31], v[236:239], v[176:179], v[16:31]
	v_exp_f32_e32 v44, v44
	v_exp_f32_e32 v45, v45
	v_exp_f32_e32 v46, v46
	v_exp_f32_e32 v47, v47
	v_cvt_pk_bf16_f32 v184, v40, v41
	v_cvt_pk_bf16_f32 v185, v42, v43
	v_mfma_f32_16x16x32_bf16 v[140:143], v[116:119], v[176:179], v[140:143]
	s_waitcnt lgkmcnt(1)
	v_mfma_f32_32x32x16_bf16 v[48:63], v[216:219], v[100:103], 0
	ds_read_b128 v[240:243], v249 offset:2048
	ds_read_b128 v[244:247], v249 offset:3072
	v_cvt_pk_bf16_f32 v186, v44, v45
	v_cvt_pk_bf16_f32 v187, v46, v47
	v_exp_f32_e32 v80, v80
	v_exp_f32_e32 v81, v81
	v_exp_f32_e32 v82, v82
	v_exp_f32_e32 v83, v83
	s_waitcnt lgkmcnt(2)
	v_mfma_f32_32x32x16_bf16 v[48:63], v[220:223], v[108:111], v[48:63]
	v_exp_f32_e32 v84, v84
	v_exp_f32_e32 v85, v85
	v_exp_f32_e32 v86, v86
	v_exp_f32_e32 v87, v87
	v_cvt_pk_bf16_f32 v172, v80, v81
	v_cvt_pk_bf16_f32 v173, v82, v83
	v_mfma_f32_16x16x32_bf16 v[136:139], v[116:119], v[180:183], v[136:139]
	v_mfma_f32_32x32x16_bf16 v[0:15], v[232:235], v[180:183], v[0:15]
	v_exp_f32_e32 v88, v88
	v_exp_f32_e32 v89, v89
	v_exp_f32_e32 v90, v90
	v_exp_f32_e32 v91, v91
	v_cvt_pk_bf16_f32 v174, v84, v85
	v_cvt_pk_bf16_f32 v175, v86, v87
	v_mfma_f32_32x32x16_bf16 v[0:15], v[236:239], v[184:187], v[0:15]
	v_exp_f32_e32 v92, v92
	v_exp_f32_e32 v93, v93
	v_exp_f32_e32 v94, v94
	v_exp_f32_e32 v95, v95
	v_cvt_pk_bf16_f32 v176, v88, v89
	v_cvt_pk_bf16_f32 v177, v90, v91
	v_mfma_f32_16x16x32_bf16 v[136:139], v[116:119], v[184:187], v[136:139]
	v_mfma_f32_32x32x16_bf16 v[32:47], v[216:219], v[104:107], 0
	ds_read_b128 v[224:227], v248 offset:6144
	ds_read_b128 v[228:231], v248 offset:7168
	v_cvt_pk_bf16_f32 v178, v92, v93
	v_cvt_pk_bf16_f32 v179, v94, v95
	v_exp_f32_e32 v64, v64
	v_exp_f32_e32 v65, v65
	v_exp_f32_e32 v66, v66
	v_exp_f32_e32 v67, v67
	v_mfma_f32_32x32x16_bf16 v[32:47], v[220:223], v[112:115], v[32:47]
	v_exp_f32_e32 v68, v68
	v_exp_f32_e32 v69, v69
	v_exp_f32_e32 v70, v70
	v_exp_f32_e32 v71, v71
	v_cvt_pk_bf16_f32 v180, v64, v65
	v_cvt_pk_bf16_f32 v181, v66, v67
	v_mfma_f32_16x16x32_bf16 v[140:143], v[116:119], v[172:175], v[140:143]
	s_waitcnt lgkmcnt(2)
	v_mfma_f32_32x32x16_bf16 v[16:31], v[240:243], v[172:175], v[16:31]
	v_exp_f32_e32 v72, v72
	v_exp_f32_e32 v73, v73
	v_exp_f32_e32 v74, v74
	v_exp_f32_e32 v75, v75
	v_cvt_pk_bf16_f32 v182, v68, v69
	v_cvt_pk_bf16_f32 v183, v70, v71
	v_mfma_f32_32x32x16_bf16 v[16:31], v[244:247], v[176:179], v[16:31]
	v_exp_f32_e32 v76, v76
	v_exp_f32_e32 v77, v77
	v_exp_f32_e32 v78, v78
	v_exp_f32_e32 v79, v79
	v_cvt_pk_bf16_f32 v184, v72, v73
	v_cvt_pk_bf16_f32 v185, v74, v75
	v_mfma_f32_16x16x32_bf16 v[140:143], v[116:119], v[176:179], v[140:143]
	s_addk_i32 s27, 0x1000
	s_cmp_lg_u32 s27, 0x10000
	s_cbranch_scc1 .Lmy_attn_loop2
	v_cvt_pk_bf16_f32 v186, v76, v77
	v_cvt_pk_bf16_f32 v187, v78, v79
	v_mfma_f32_32x32x16_bf16 v[0:15], v[240:243], v[180:183], v[0:15]
	s_nop 0
	v_mfma_f32_16x16x32_bf16 v[136:139], v[116:119], v[180:183], v[136:139]
	v_mfma_f32_32x32x16_bf16 v[0:15], v[244:247], v[184:187], v[0:15]
	s_nop 0
	s_nop 1
	v_mfma_f32_16x16x32_bf16 v[136:139], v[116:119], v[184:187], v[136:139]
	s_setprio 0
	v_lshrrev_b32_e32 v60, 2, v158
	v_and_b32_e32 v60, 60, v60
	v_and_b32_e32 v61, 0x100, v158
	v_lshrrev_b32_e32 v61, 1, v61
	v_or_b32_e32 v60, v60, v61
	s_nop 4
	ds_bpermute_b32 v61, v60, v136
	ds_bpermute_b32 v62, v60, v140
	s_waitcnt lgkmcnt(0)
	v_mul_f32_e32 v136, 0.5, v61
	v_mul_f32_e32 v140, 0.5, v62
	v_or_b32_e32 v34, 0x20800, v158
	ds_read_b128 v[116:119], v34
	v_or_b32_e32 v36, 0x20c00, v158
	s_mov_b32 s4, 0x3f803f80
	v_exp_f32_e32 v35, v49
	ds_read_b128 v[120:123], v36
	v_exp_f32_e32 v34, v48
	s_mov_b32 s5, s4
	v_mov_b64_e32 v[46:47], s[4:5]
	v_exp_f32_e32 v38, v32
	v_exp_f32_e32 v39, v33
	v_cndmask_b32_e64 v34, 0, v34, s[0:1]
	v_cndmask_b32_e64 v35, 0, v35, s[0:1]
	v_mov_b32_e32 v125, 0
	v_cvt_pk_bf16_f32 v124, v34, v35
	v_mov_b32_e32 v126, v125
	v_mov_b32_e32 v127, v125
	v_cndmask_b32_e64 v38, 0, v38, s[0:1]
	v_cndmask_b32_e64 v39, 0, v39, s[0:1]
	s_waitcnt lgkmcnt(1)
	v_mfma_f32_32x32x16_bf16 v[16:31], v[116:119], v[124:127], v[16:31]
	s_mov_b32 s8, 0
	s_mov_b32 s9, s8
	v_mov_b64_e32 v[36:37], s[8:9]
	s_mov_b32 s10, s8
	s_mov_b32 s11, s8
	v_mov_b64_e32 v[44:45], s[10:11]
	v_mov_b64_e32 v[42:43], s[8:9]
	v_mfma_f32_4x4x4_16b_bf16 v[32:35], v[46:47], v[124:125], v[140:143]
	v_cvt_pk_bf16_f32 v124, v38, v39
	s_waitcnt lgkmcnt(0)
	v_mfma_f32_32x32x16_bf16 v[16:31], v[120:123], v[42:45], v[16:31]
	s_mov_b32 s9, 0x7149f2ca
	s_mov_b32 s6, 0xda24260
	v_mfma_f32_32x32x16_bf16 v[0:15], v[116:119], v[124:127], v[0:15]
	v_mfma_f32_4x4x4_16b_bf16 v[38:41], v[46:47], v[36:37], v[32:35]
	v_mfma_f32_4x4x4_16b_bf16 v[32:35], v[46:47], v[124:125], v[136:139]
	v_mfma_f32_32x32x16_bf16 v[0:15], v[120:123], v[42:45], v[0:15]
	s_nop 0
	v_mfma_f32_4x4x4_16b_bf16 v[32:35], v[46:47], v[36:37], v[32:35]
	s_nop 4
	ds_bpermute_b32 v35, v165, v38
	ds_bpermute_b32 v34, v165, v32
	v_mov_b32_e32 v33, v38
	s_waitcnt lgkmcnt(0)
	v_pk_add_f32 v[34:35], v[32:33], v[34:35]
	s_nop 0
	v_cmp_ngt_f32_e32 vcc, s9, v35
	v_cmp_nlt_f32_e64 s[4:5], s6, v34
	v_cmp_nlt_f32_e64 s[6:7], s6, v35
	s_or_b64 s[6:7], s[6:7], vcc
	v_cmp_ngt_f32_e32 vcc, s9, v34
	s_or_b64 s[4:5], s[4:5], vcc
	s_or_b64 vcc, s[6:7], s[4:5]
	s_cbranch_vccnz .LBB6_64
